# grid barrier: the XCD's first arriver starts an L2 write-back right after arriving (off the critical path)
# baseline (speedup 1.0000x reference)
; __device__ __forceinline__ unsigned xb_add(unsigned* p, unsigned v) { return __hip_atomic_fetch_add(p, v, __ATOMIC_RELAXED, __HIP_MEMORY_SCOPE_AGENT); }
; __device__ __forceinline__ void xcd_barrier(const XcdBarrier& b) {
;     ...
;         const unsigned old = xb_add(&bar[XB_XSUB(b.x)], 1u);
;         const unsigned gen = old / nloc;
;         if (old + 1u == (gen + 1u) * nloc) {
.LBB0_40:
	s_lshl_b32 s3, s82, 8
	s_add_u32 s6, s80, s3
	s_addc_u32 s7, s81, 0
	v_mov_b32_e32 v2, 0x1000
	v_mov_b32_e32 v4, 1
	global_atomic_add v4, v2, v4, s[6:7] offset:1024 sc0
	v_cvt_f32_u32_e32 v2, v3
	v_sub_u32_e32 v5, 0, v3
	v_rcp_iflag_f32_e32 v2, v2
	s_nop 0
	v_mul_f32_e32 v2, 0x4f7ffffe, v2
	v_cvt_u32_f32_e32 v2, v2
	v_mul_lo_u32 v5, v5, v2
	v_mul_hi_u32 v5, v2, v5
	v_add_u32_e32 v2, v2, v5
	s_waitcnt vmcnt(0)
	v_mul_hi_u32 v2, v4, v2
	v_mul_lo_u32 v5, v2, v3
	v_sub_u32_e32 v5, v4, v5
	v_add_u32_e32 v6, 1, v2
	v_cmp_ge_u32_e32 vcc, v5, v3
	v_add_u32_e32 v4, 1, v4
	s_nop 0
	v_cndmask_b32_e32 v2, v2, v6, vcc
	v_sub_u32_e32 v6, v5, v3
	v_cndmask_b32_e32 v5, v5, v6, vcc
	v_add_u32_e32 v6, 1, v2
	v_cmp_ge_u32_e32 vcc, v5, v3
	s_nop 1
	v_cndmask_b32_e32 v2, v2, v6, vcc
	v_mul_lo_u32 v5, v3, v2
	v_add_u32_e32 v3, v5, v3
	v_cmp_ne_u32_e32 vcc, v4, v3
	s_and_saveexec_b64 s[8:9], vcc
	s_xor_b64 s[8:9], exec, s[8:9]
	s_cbranch_execz .LBB0_54
	v_add_u32_e32 v20, 1, v5
	v_cmp_eq_u32_e32 vcc, v4, v20
	s_cbranch_vccz .Lfwb0
	buffer_wbl2 sc1
.Lfwb0:
	s_waitcnt lgkmcnt(0)
	v_add_u32_e32 v19, 1, v2
	v_mul_lo_u32 v19, v19, v1
	v_mov_b32_e32 v1, 0x7000
	global_load_dword v1, v1, s[90:91] offset:1024 sc1
	s_add_u32 s14, s90, 0x7400
	s_addc_u32 s15, s91, 0
	s_waitcnt vmcnt(0)
	v_cmp_lt_u32_e32 vcc, v1, v19
	s_and_saveexec_b64 s[10:11], vcc
	s_cbranch_execz .LBB0_53
	s_add_u32 s12, s90, 0x4200
	s_addc_u32 s13, s91, 0
	s_mov_b32 s3, 1
	s_mov_b64 s[26:27], 0
	v_mov_b32_e32 v1, 0
	s_branch .LBB0_44

; __device__ __forceinline__ unsigned xb_add(unsigned* p, unsigned v) { return __hip_atomic_fetch_add(p, v, __ATOMIC_RELAXED, __HIP_MEMORY_SCOPE_AGENT); }
; __device__ __forceinline__ void xcd_barrier(const XcdBarrier& b) {
;     ...
;         const unsigned old = xb_add(&bar[XB_XSUB(b.x)], 1u);
;         const unsigned gen = old / nloc;
;         if (old + 1u == (gen + 1u) * nloc) {
.LBB0_168:
	s_lshl_b32 s3, s82, 8
	s_add_u32 s4, s80, s3
	s_addc_u32 s5, s81, 0
	v_mov_b32_e32 v2, 0x1000
	v_mov_b32_e32 v4, 1
	global_atomic_add v4, v2, v4, s[4:5] offset:1024 sc0
	v_cvt_f32_u32_e32 v2, v3
	v_sub_u32_e32 v5, 0, v3
	v_rcp_iflag_f32_e32 v2, v2
	s_nop 0
	v_mul_f32_e32 v2, 0x4f7ffffe, v2
	v_cvt_u32_f32_e32 v2, v2
	v_mul_lo_u32 v5, v5, v2
	v_mul_hi_u32 v5, v2, v5
	v_add_u32_e32 v2, v2, v5
	s_waitcnt vmcnt(0)
	v_mul_hi_u32 v2, v4, v2
	v_mul_lo_u32 v5, v2, v3
	v_sub_u32_e32 v5, v4, v5
	v_add_u32_e32 v6, 1, v2
	v_cmp_ge_u32_e32 vcc, v5, v3
	v_add_u32_e32 v4, 1, v4
	s_nop 0
	v_cndmask_b32_e32 v2, v2, v6, vcc
	v_sub_u32_e32 v6, v5, v3
	v_cndmask_b32_e32 v5, v5, v6, vcc
	v_add_u32_e32 v6, 1, v2
	v_cmp_ge_u32_e32 vcc, v5, v3
	s_nop 1
	v_cndmask_b32_e32 v2, v2, v6, vcc
	v_mul_lo_u32 v5, v3, v2
	v_add_u32_e32 v3, v5, v3
	v_cmp_ne_u32_e32 vcc, v4, v3
	s_and_saveexec_b64 s[6:7], vcc
	s_xor_b64 s[6:7], exec, s[6:7]
	s_cbranch_execz .LBB0_182
	v_add_u32_e32 v20, 1, v5
	v_cmp_eq_u32_e32 vcc, v4, v20
	s_cbranch_vccz .Lfwb1
	buffer_wbl2 sc1
.Lfwb1:
	s_waitcnt lgkmcnt(0)
	v_add_u32_e32 v19, 1, v2
	v_mul_lo_u32 v19, v19, v1
	v_mov_b32_e32 v1, 0x7000
	global_load_dword v1, v1, s[90:91] offset:1024 sc1
	s_add_u32 s12, s90, 0x7400
	s_addc_u32 s13, s91, 0
	s_waitcnt vmcnt(0)
	v_cmp_lt_u32_e32 vcc, v1, v19
	s_and_saveexec_b64 s[8:9], vcc
	s_cbranch_execz .LBB0_181
	s_add_u32 s10, s90, 0x4200
	s_addc_u32 s11, s91, 0
	s_mov_b32 s3, 1
	s_mov_b64 s[14:15], 0
	v_mov_b32_e32 v1, 0
	s_branch .LBB0_172

; __device__ __forceinline__ unsigned xb_ld(unsigned* p)              { return __hip_atomic_load(p, __ATOMIC_RELAXED, __HIP_MEMORY_SCOPE_AGENT); }
; __device__ __forceinline__ unsigned xb_add(unsigned* p, unsigned v) { return __hip_atomic_fetch_add(p, v, __ATOMIC_RELAXED, __HIP_MEMORY_SCOPE_AGENT); }
; #define XB_SPIN(cond, bar) do { unsigned _sp = 0; while (cond) { __builtin_amdgcn_s_sleep(1); \
;     if ((++_sp & 255u) == 0u) { if (xb_ld(&(bar)[XB_TMO])) break; if (_sp > XB_SPIN_CAP) { atomicAdd(&(bar)[XB_TMO], 1u); break; } } } } while (0)
; __device__ __forceinline__ void xcd_barrier(const XcdBarrier& b) {
;     ...
;         const unsigned old = xb_add(&bar[XB_XSUB(b.x)], 1u);
;         const unsigned gen = old / nloc;
;         if (old + 1u == (gen + 1u) * nloc) {
;             __builtin_amdgcn_fence(__ATOMIC_RELEASE, "agent");
;             asm volatile("s_waitcnt vmcnt(0)" ::: "memory");
;             const unsigned og = xb_add(&bar[XB_TOP], 1u);
;             const unsigned tg = og / nx;
;             if (og + 1u == (tg + 1u) * nx) xb_add(&bar[XB_TOPGEN], 1u);
;             else XB_SPIN(xb_ld(&bar[XB_TOPGEN]) == tg, bar);
.LBB0_1196:
	s_lshl_b32 s3, s82, 8
	s_add_u32 s8, s80, s3
	s_addc_u32 s9, s81, 0
	v_mov_b32_e32 v2, 0x1000
	v_mov_b32_e32 v4, 1
	global_atomic_add v4, v2, v4, s[8:9] offset:1024 sc0
	v_cvt_f32_u32_e32 v2, v3
	v_sub_u32_e32 v5, 0, v3
	v_rcp_iflag_f32_e32 v2, v2
	s_nop 0
	v_mul_f32_e32 v2, 0x4f7ffffe, v2
	v_cvt_u32_f32_e32 v2, v2
	v_mul_lo_u32 v5, v5, v2
	v_mul_hi_u32 v5, v2, v5
	v_add_u32_e32 v2, v2, v5
	s_waitcnt vmcnt(0)
	v_mul_hi_u32 v2, v4, v2
	v_mul_lo_u32 v5, v2, v3
	v_sub_u32_e32 v5, v4, v5
	v_add_u32_e32 v6, 1, v2
	v_cmp_ge_u32_e32 vcc, v5, v3
	v_add_u32_e32 v4, 1, v4
	s_nop 0
	v_cndmask_b32_e32 v2, v2, v6, vcc
	v_sub_u32_e32 v6, v5, v3
	v_cndmask_b32_e32 v5, v5, v6, vcc
	v_add_u32_e32 v6, 1, v2
	v_cmp_ge_u32_e32 vcc, v5, v3
	s_nop 1
	v_cndmask_b32_e32 v2, v2, v6, vcc
	v_mul_lo_u32 v5, v3, v2
	v_add_u32_e32 v3, v5, v3
	v_cmp_ne_u32_e32 vcc, v4, v3
	s_and_saveexec_b64 s[10:11], vcc
	s_xor_b64 s[10:11], exec, s[10:11]
	s_cbranch_execz .LBB0_1210
	v_add_u32_e32 v20, 1, v5
	v_cmp_eq_u32_e32 vcc, v4, v20
	s_cbranch_vccz .Lfwb10
	buffer_wbl2 sc1
.Lfwb10:
	s_waitcnt lgkmcnt(0)
	v_add_u32_e32 v19, 1, v2
	v_mul_lo_u32 v19, v19, v1
	v_mov_b32_e32 v1, 0x7000
	global_load_dword v1, v1, s[90:91] offset:1024 sc1
	s_add_u32 s16, s90, 0x7400
	s_addc_u32 s17, s91, 0
	s_waitcnt vmcnt(0)
	v_cmp_lt_u32_e32 vcc, v1, v19
	s_and_saveexec_b64 s[12:13], vcc
	s_cbranch_execz .LBB0_1209
	s_add_u32 s14, s90, 0x4200
	s_addc_u32 s15, s91, 0
	s_mov_b32 s3, 1
	s_mov_b64 s[18:19], 0
	v_mov_b32_e32 v1, 0
	s_branch .LBB0_1200

; __device__ __forceinline__ unsigned xb_ld(unsigned* p)              { return __hip_atomic_load(p, __ATOMIC_RELAXED, __HIP_MEMORY_SCOPE_AGENT); }
; __device__ __forceinline__ unsigned xb_add(unsigned* p, unsigned v) { return __hip_atomic_fetch_add(p, v, __ATOMIC_RELAXED, __HIP_MEMORY_SCOPE_AGENT); }
; #define XB_SPIN(cond, bar) do { unsigned _sp = 0; while (cond) { __builtin_amdgcn_s_sleep(1); \
;     if ((++_sp & 255u) == 0u) { if (xb_ld(&(bar)[XB_TMO])) break; if (_sp > XB_SPIN_CAP) { atomicAdd(&(bar)[XB_TMO], 1u); break; } } } } while (0)
; __device__ __forceinline__ void xcd_barrier(const XcdBarrier& b) {
;     ...
;         const unsigned old = xb_add(&bar[XB_XSUB(b.x)], 1u);
;         const unsigned gen = old / nloc;
;         if (old + 1u == (gen + 1u) * nloc) {
;             __builtin_amdgcn_fence(__ATOMIC_RELEASE, "agent");
;             asm volatile("s_waitcnt vmcnt(0)" ::: "memory");
;             const unsigned og = xb_add(&bar[XB_TOP], 1u);
;             const unsigned tg = og / nx;
;             if (og + 1u == (tg + 1u) * nx) xb_add(&bar[XB_TOPGEN], 1u);
;             else XB_SPIN(xb_ld(&bar[XB_TOPGEN]) == tg, bar);
.LBB0_1262:
	s_lshl_b32 s0, s82, 8
	s_add_u32 s0, s80, s0
	s_addc_u32 s1, s81, 0
	v_mov_b32_e32 v2, 0x1000
	v_mov_b32_e32 v4, 1
	global_atomic_add v4, v2, v4, s[0:1] offset:1024 sc0
	v_cvt_f32_u32_e32 v2, v3
	v_sub_u32_e32 v5, 0, v3
	v_rcp_iflag_f32_e32 v2, v2
	s_nop 0
	v_mul_f32_e32 v2, 0x4f7ffffe, v2
	v_cvt_u32_f32_e32 v2, v2
	v_mul_lo_u32 v5, v5, v2
	v_mul_hi_u32 v5, v2, v5
	v_add_u32_e32 v2, v2, v5
	s_waitcnt vmcnt(0)
	v_mul_hi_u32 v2, v4, v2
	v_mul_lo_u32 v5, v2, v3
	v_sub_u32_e32 v5, v4, v5
	v_add_u32_e32 v6, 1, v2
	v_cmp_ge_u32_e32 vcc, v5, v3
	v_add_u32_e32 v4, 1, v4
	s_nop 0
	v_cndmask_b32_e32 v2, v2, v6, vcc
	v_sub_u32_e32 v6, v5, v3
	v_cndmask_b32_e32 v5, v5, v6, vcc
	v_add_u32_e32 v6, 1, v2
	v_cmp_ge_u32_e32 vcc, v5, v3
	s_nop 1
	v_cndmask_b32_e32 v2, v2, v6, vcc
	v_mul_lo_u32 v5, v3, v2
	v_add_u32_e32 v3, v5, v3
	v_cmp_ne_u32_e32 vcc, v4, v3
	s_and_saveexec_b64 s[6:7], vcc
	s_xor_b64 s[6:7], exec, s[6:7]
	s_cbranch_execz .LBB0_1276
	v_add_u32_e32 v20, 1, v5
	v_cmp_eq_u32_e32 vcc, v4, v20
	s_cbranch_vccz .Lfwb11
	buffer_wbl2 sc1
